# speedup vs baseline: 1.0264x; 1.0264x over previous
_Z16sum_layer_kernelPKfS0_Pf:
	s_load_dwordx4 s[4:7], s[0:1], 0x0
	s_load_dwordx2 s[8:9], s[0:1], 0x10
	v_and_b32_e32 v40, 31, v0
	v_bfe_u32 v41, v0, 5, 1
	v_lshrrev_b32_e32 v42, 6, v0
	v_and_b32_e32 v43, 7, v0
	v_bfe_u32 v44, v0, 3, 3
	v_and_b32_e32 v45, 63, v0
	s_lshl_b32 s3, s2, 12
	s_lshl_b32 s19, s2, 7
	v_lshlrev_b32_e32 v1, 11, v41
	v_lshl_or_b32 v1, v40, 2, v1
	v_lshlrev_b32_e32 v46, 4, v43
	v_lshl_add_u32 v35, v44, 16, v46
	v_lshl_add_u32 v35, v42, 21, v35
	v_add_u32_e32 v35, s19, v35
	v_lshlrev_b32_e32 v36, 2, v40
	v_lshl_add_u32 v36, v41, 18, v36
	v_lshl_add_u32 v36, v42, 21, v36
	v_add_u32_e32 v36, s19, v36
	v_mul_u32_u24_e32 v37, 0x1200, v42
	v_mul_u32_u24_e32 v38, 0x90, v44
	v_add3_u32 v38, v37, v38, v46
	v_mul_u32_u24_e32 v39, 0x90, v40
	v_lshlrev_b32_e32 v47, 6, v41
	v_add3_u32 v39, v37, v39, v47
	v_lshrrev_b32_e32 v46, 1, v44
	v_xor_b32_e32 v46, v43, v46
	v_lshlrev_b32_e32 v46, 4, v46
	v_lshl_add_u32 v35, v44, 16, v46
	v_lshl_add_u32 v35, v42, 21, v35
	v_add_u32_e32 v35, s19, v35
	v_xor_b32_e32 v86, 64, v35
	v_readfirstlane_b32 s23, v42
	v_bfe_u32 v47, v40, 1, 3
	v_lshlrev_b32_e32 v39, 2, v41
	v_xor_b32_e32 v39, v39, v47
	s_lshl_b32 s44, s23, 10
	s_add_u32 s44, s44, 0x4000
	s_lshl_b32 s46, s23, 9
	s_add_u32 s46, s46, s3
	v_lshlrev_b32_e32 v84, 2, v45
	v_add_u32_e32 v84, 0x4000, v84
	s_lshl_b32 s23, s23, 12
	v_lshlrev_b32_e32 v39, 4, v39
	v_lshl_add_u32 v39, v40, 7, v39
	v_lshl_add_u32 v39, v42, 12, v39
	s_mov_b32 m0, s23
	v_xor_b32_e32 v81, 16, v39
	v_xor_b32_e32 v82, 32, v39
	v_xor_b32_e32 v83, 48, v39
	v_cmp_gt_u32_e32 vcc, 32, v45
	v_mov_b32_e32 v34, 0xc1600000
	s_mov_b32 s16, 0x3fb8aa3b
	s_mov_b32 s17, 0x3f317218
	s_mov_b32 s20, 0x7fc00
	s_mov_b32 s21, 0xff800
	s_mov_b32 s22, 0x17f400
	s_lshl_b32 s24, 1, 16
	s_lshl_b32 s25, 2, 16
	s_lshl_b32 s26, 3, 16
	s_lshl_b32 s27, 8, 16
	s_lshl_b32 s28, 9, 16
	s_lshl_b32 s29, 10, 16
	s_lshl_b32 s30, 11, 16
	s_lshl_b32 s31, 16, 16
	s_lshl_b32 s32, 17, 16
	s_lshl_b32 s33, 18, 16
	s_lshl_b32 s34, 19, 16
	s_lshl_b32 s35, 24, 16
	s_lshl_b32 s36, 25, 16
	s_lshl_b32 s37, 26, 16
	s_lshl_b32 s38, 27, 16
	s_mov_b32 s14, 0x200000
	s_mov_b32 s15, 0x20000
	s_waitcnt lgkmcnt(0)
	s_mov_b32 s12, s6
	s_and_b32 s13, s7, 0xffff
	s_and_b32 s5, s5, 0xffff
	s_mov_b32 s6, 0x800000
	s_mov_b32 s7, s15
	s_and_b32 s9, s9, 0xffff
	s_mov_b32 s10, s6
	s_mov_b32 s11, s15
	s_mov_b32 m0, s44
	s_nop 0
	buffer_load_dword v1, s[12:15], s46 offen nt lds
	s_add_u32 m0, s44, 128
	s_nop 0
	buffer_load_dword v1, s[12:15], s46 offen offset:128 nt lds
	s_add_u32 m0, s44, 256
	s_nop 0
	buffer_load_dword v1, s[12:15], s46 offen offset:256 nt lds
	s_add_u32 m0, s44, 384
	s_nop 0
	buffer_load_dword v1, s[12:15], s46 offen offset:384 nt lds
	s_mov_b32 m0, s23
	s_nop 0
	buffer_load_dwordx4 v35, s[4:7], 0 offen nt lds
	buffer_load_dwordx4 v86, s[4:7], s20 offen offset:1024 nt lds
	buffer_load_dwordx4 v35, s[4:7], s21 offen offset:2048 nt lds
	buffer_load_dwordx4 v86, s[4:7], s22 offen offset:3072 nt lds
	s_waitcnt vmcnt(4)
	s_barrier
	ds_read2st64_b32 v[18:19], v84 offset0:0 offset1:1
	ds_read2st64_b32 v[20:21], v84 offset0:2 offset1:3
	ds_read2st64_b32 v[22:23], v84 offset0:4 offset1:5
	ds_read2st64_b32 v[24:25], v84 offset0:6 offset1:7
	ds_read2st64_b32 v[26:27], v84 offset0:8 offset1:9
	ds_read2st64_b32 v[28:29], v84 offset0:10 offset1:11
	ds_read2st64_b32 v[30:31], v84 offset0:12 offset1:13
	ds_read2st64_b32 v[32:33], v84 offset0:14 offset1:15
	s_waitcnt lgkmcnt(0)
	v_max3_f32 v49, v18, v19, v20
	v_max3_f32 v50, v21, v22, v23
	v_max3_f32 v49, v49, v24, v25
	v_max3_f32 v50, v50, v26, v27
	v_max3_f32 v49, v49, v28, v29
	v_max3_f32 v50, v50, v30, v31
	v_max3_f32 v49, v49, v32, v33
	v_max_f32_e32 v49, v49, v50
	v_mov_b32_e32 v50, v49
	s_nop 1
	v_permlane32_swap_b32_e32 v49, v50
	v_max_f32_e32 v49, v49, v50
	v_fmamk_f32 v49, v49, 0x3fb8aa3b, v34
	v_fma_f32 v18, v18, s16, -v49
	v_exp_f32_e32 v18, v18
	v_fma_f32 v19, v19, s16, -v49
	v_exp_f32_e32 v19, v19
	v_fma_f32 v20, v20, s16, -v49
	v_exp_f32_e32 v20, v20
	v_fma_f32 v21, v21, s16, -v49
	v_exp_f32_e32 v21, v21
	v_fma_f32 v22, v22, s16, -v49
	v_exp_f32_e32 v22, v22
	v_fma_f32 v23, v23, s16, -v49
	v_exp_f32_e32 v23, v23
	v_fma_f32 v24, v24, s16, -v49
	v_exp_f32_e32 v24, v24
	v_fma_f32 v25, v25, s16, -v49
	v_exp_f32_e32 v25, v25
	v_fma_f32 v26, v26, s16, -v49
	v_exp_f32_e32 v26, v26
	v_fma_f32 v27, v27, s16, -v49
	v_exp_f32_e32 v27, v27
	v_fma_f32 v28, v28, s16, -v49
	v_exp_f32_e32 v28, v28
	v_fma_f32 v29, v29, s16, -v49
	v_exp_f32_e32 v29, v29
	v_fma_f32 v30, v30, s16, -v49
	v_exp_f32_e32 v30, v30
	v_fma_f32 v31, v31, s16, -v49
	v_exp_f32_e32 v31, v31
	v_fma_f32 v32, v32, s16, -v49
	v_exp_f32_e32 v32, v32
	v_fma_f32 v33, v33, s16, -v49
	v_exp_f32_e32 v33, v33
	v_add_f32_e32 v50, v18, v19
	v_add_f32_e32 v51, v20, v21
	v_add_f32_e32 v50, v50, v22
	v_add_f32_e32 v51, v51, v23
	v_add_f32_e32 v50, v50, v24
	v_add_f32_e32 v51, v51, v25
	v_add_f32_e32 v50, v50, v26
	v_add_f32_e32 v51, v51, v27
	v_add_f32_e32 v50, v50, v28
	v_add_f32_e32 v51, v51, v29
	v_add_f32_e32 v50, v50, v30
	v_add_f32_e32 v51, v51, v31
	v_add_f32_e32 v50, v50, v32
	v_add_f32_e32 v51, v51, v33
	v_add_f32_e32 v50, v50, v51
	v_mov_b32_e32 v51, v50
	s_nop 1
	v_permlane32_swap_b32_e32 v50, v51
	v_add_f32_e32 v50, v50, v51
	v_log_f32_e32 v50, v50
	v_cvt_pk_f16_f32 v40, v18, v19
	v_cvt_pk_f16_f32 v41, v20, v21
	v_cvt_pk_f16_f32 v42, v22, v23
	v_cvt_pk_f16_f32 v43, v24, v25
	v_cvt_pk_f16_f32 v44, v26, v27
	v_cvt_pk_f16_f32 v45, v28, v29
	v_cvt_pk_f16_f32 v46, v30, v31
	v_cvt_pk_f16_f32 v47, v32, v33
	v_add_f32_e32 v50, 0x41600000, v50
	v_mul_f32_e32 v50, 0xbf317218, v50
	v_cndmask_b32_e64 v51, v50, 1.0, vcc
	s_waitcnt vmcnt(0)
	ds_read_b128 v[2:5], v39
	ds_read_b128 v[6:9], v81
	ds_read_b128 v[10:13], v82
	ds_read_b128 v[14:17], v83
	s_waitcnt lgkmcnt(2)
	v_max3_f32 v52, v2, v3, v4
	v_max3_f32 v53, v5, v6, v7
	v_max_f32_e32 v52, v52, v8
	v_max_f32_e32 v53, v53, v9
	s_waitcnt lgkmcnt(0)
	v_max3_f32 v52, v52, v10, v11
	v_max3_f32 v53, v53, v12, v13
	v_max3_f32 v52, v52, v14, v15
	v_max3_f32 v53, v53, v16, v17
	v_max_f32_e32 v52, v52, v53
	v_mov_b32_e32 v53, v52
	s_nop 1
	v_permlane32_swap_b32_e32 v52, v53
	v_max_f32_e32 v52, v52, v53
	v_cndmask_b32_e32 v54, 1.0, v52, vcc
	v_fmamk_f32 v55, v52, 0x3fb8aa3b, v34
	v_fma_f32 v2, v2, s16, -v55
	v_mfma_f32_32x32x2_f32 v[64:79], v54, v51, 0
	v_exp_f32_e32 v2, v2
	v_fma_f32 v3, v3, s16, -v55
	v_exp_f32_e32 v3, v3
	v_fma_f32 v4, v4, s16, -v55
	v_exp_f32_e32 v4, v4
	v_fma_f32 v5, v5, s16, -v55
	v_exp_f32_e32 v5, v5
	v_fma_f32 v6, v6, s16, -v55
	v_exp_f32_e32 v6, v6
	v_fma_f32 v7, v7, s16, -v55
	v_exp_f32_e32 v7, v7
	v_fma_f32 v8, v8, s16, -v55
	v_exp_f32_e32 v8, v8
	v_fma_f32 v9, v9, s16, -v55
	v_exp_f32_e32 v9, v9
	v_fma_f32 v10, v10, s16, -v55
	v_exp_f32_e32 v10, v10
	v_cvt_pk_f16_f32 v56, v2, v3
	v_cvt_pk_f16_f32 v57, v4, v5
	v_cvt_pk_f16_f32 v58, v6, v7
	v_cvt_pk_f16_f32 v59, v8, v9
	v_fma_f32 v11, v11, s16, -v55
	v_exp_f32_e32 v11, v11
	v_fma_f32 v12, v12, s16, -v55
	v_exp_f32_e32 v12, v12
	v_mfma_f32_32x32x16_f16 v[18:33], v[56:59], v[40:43], 0
	v_fma_f32 v13, v13, s16, -v55
	v_exp_f32_e32 v13, v13
	v_fma_f32 v14, v14, s16, -v55
	v_exp_f32_e32 v14, v14
	v_fma_f32 v15, v15, s16, -v55
	v_exp_f32_e32 v15, v15
	v_fma_f32 v16, v16, s16, -v55
	v_exp_f32_e32 v16, v16
	v_fma_f32 v17, v17, s16, -v55
	v_exp_f32_e32 v17, v17
	v_cvt_pk_f16_f32 v60, v10, v11
	v_cvt_pk_f16_f32 v61, v12, v13
	v_cvt_pk_f16_f32 v62, v14, v15
	v_cvt_pk_f16_f32 v63, v16, v17
	s_nop 1
	v_mfma_f32_32x32x16_f16 v[18:33], v[60:63], v[44:47], v[18:33]
	s_nop 11
	v_log_f32_e32 v18, v18
	v_log_f32_e32 v19, v19
	v_log_f32_e32 v20, v20
	v_fmac_f32_e32 v64, s17, v18
	buffer_store_dword v64, v36, s[8:11], 0 offen
	v_log_f32_e32 v21, v21
	v_fmac_f32_e32 v65, s17, v19
	buffer_store_dword v65, v36, s[8:11], s24 offen
	v_log_f32_e32 v22, v22
	v_fmac_f32_e32 v66, s17, v20
	buffer_store_dword v66, v36, s[8:11], s25 offen
	v_log_f32_e32 v23, v23
	v_fmac_f32_e32 v67, s17, v21
	buffer_store_dword v67, v36, s[8:11], s26 offen
	v_log_f32_e32 v24, v24
	v_fmac_f32_e32 v68, s17, v22
	buffer_store_dword v68, v36, s[8:11], s27 offen
	v_log_f32_e32 v25, v25
	v_fmac_f32_e32 v69, s17, v23
	buffer_store_dword v69, v36, s[8:11], s28 offen
	v_log_f32_e32 v26, v26
	v_fmac_f32_e32 v70, s17, v24
	buffer_store_dword v70, v36, s[8:11], s29 offen
	v_log_f32_e32 v27, v27
	v_fmac_f32_e32 v71, s17, v25
	buffer_store_dword v71, v36, s[8:11], s30 offen
	v_log_f32_e32 v28, v28
	v_fmac_f32_e32 v72, s17, v26
	buffer_store_dword v72, v36, s[8:11], s31 offen
	v_log_f32_e32 v29, v29
	v_fmac_f32_e32 v73, s17, v27
	buffer_store_dword v73, v36, s[8:11], s32 offen
	v_log_f32_e32 v30, v30
	v_fmac_f32_e32 v74, s17, v28
	buffer_store_dword v74, v36, s[8:11], s33 offen
	v_log_f32_e32 v31, v31
	v_fmac_f32_e32 v75, s17, v29
	buffer_store_dword v75, v36, s[8:11], s34 offen
	v_log_f32_e32 v32, v32
	v_fmac_f32_e32 v76, s17, v30
	buffer_store_dword v76, v36, s[8:11], s35 offen
	v_log_f32_e32 v33, v33
	v_fmac_f32_e32 v77, s17, v31
	buffer_store_dword v77, v36, s[8:11], s36 offen
	v_fmac_f32_e32 v78, s17, v32
	buffer_store_dword v78, v36, s[8:11], s37 offen
	v_fmac_f32_e32 v79, s17, v33
	buffer_store_dword v79, v36, s[8:11], s38 offen
	s_endpgm

	.amdhsa_kernel _Z16sum_layer_kernelPKfS0_Pf
		.amdhsa_group_segment_fixed_size 20480
		.amdhsa_private_segment_fixed_size 0
		.amdhsa_kernarg_size 24
		.amdhsa_user_sgpr_count 2
		.amdhsa_user_sgpr_dispatch_ptr 0
		.amdhsa_user_sgpr_queue_ptr 0
		.amdhsa_user_sgpr_kernarg_segment_ptr 1
		.amdhsa_user_sgpr_dispatch_id 0
		.amdhsa_user_sgpr_kernarg_preload_length 0
		.amdhsa_user_sgpr_kernarg_preload_offset 0
		.amdhsa_user_sgpr_private_segment_size 0
		.amdhsa_uses_dynamic_stack 0
		.amdhsa_enable_private_segment 0
		.amdhsa_system_sgpr_workgroup_id_x 1
		.amdhsa_system_sgpr_workgroup_id_y 0
		.amdhsa_system_sgpr_workgroup_id_z 0
		.amdhsa_system_sgpr_workgroup_info 0
		.amdhsa_system_vgpr_workitem_id 0
		.amdhsa_next_free_vgpr 88
		.amdhsa_next_free_sgpr 47
		.amdhsa_accum_offset 88
		.amdhsa_reserve_vcc 1
		.amdhsa_float_round_mode_32 0
		.amdhsa_float_round_mode_16_64 0
		.amdhsa_float_denorm_mode_32 3
		.amdhsa_float_denorm_mode_16_64 3
		.amdhsa_dx10_clamp 1
		.amdhsa_ieee_mode 1
		.amdhsa_fp16_overflow 0
		.amdhsa_tg_split 0
		.amdhsa_exception_fp_ieee_invalid_op 0
		.amdhsa_exception_fp_denorm_src 0
		.amdhsa_exception_fp_ieee_div_zero 0
		.amdhsa_exception_fp_ieee_overflow 0
		.amdhsa_exception_fp_ieee_underflow 0
		.amdhsa_exception_fp_ieee_inexact 0
		.amdhsa_exception_int_div_zero 0
	.end_amdhsa_kernel

amdhsa.kernels:
  - .agpr_count:     0
    .args:
      - .address_space:  global
        .offset:         0
        .size:           8
        .value_kind:     global_buffer
      - .address_space:  global
        .offset:         8
        .size:           8
        .value_kind:     global_buffer
      - .address_space:  global
        .offset:         16
        .size:           8
        .value_kind:     global_buffer
    .group_segment_fixed_size: 20480
    .kernarg_segment_align: 8
    .kernarg_segment_size: 24
    .language:       OpenCL C
    .language_version:
      - 2
      - 0
    .max_flat_workgroup_size: 256
    .name:           _Z16sum_layer_kernelPKfS0_Pf
    .private_segment_fixed_size: 0
    .sgpr_count:     53
    .sgpr_spill_count: 0
    .symbol:         _Z16sum_layer_kernelPKfS0_Pf.kd
    .uniform_work_group_size: 1
    .uses_dynamic_stack: false
    .vgpr_count:     88
    .vgpr_spill_count: 0
    .wavefront_size: 64
